# kmean phase: all 32 row loads of an item in flight (hipcc's mid-burst vmcnt(0..5) waits moved behind the last load) on top of the barrier early-invalidate + MoBA QK prefetch version
# baseline (speedup 1.0000x reference)
.LBB0_417:
	s_ashr_i32 s5, s4, 31
	s_lshr_b32 s0, s5, 27
	s_add_i32 s0, s4, s0
	s_ashr_i32 s0, s0, 5
	s_lshl_b32 s1, s0, 13
	s_sub_i32 s1, s7, s1
	s_mul_hi_i32 s9, s1, 0x3000
	s_mulk_i32 s1, 0x3000
	s_add_u32 s10, s80, s1
	s_addc_u32 s9, s81, s9
	s_lshl_b32 s0, s0, 7
	s_ashr_i32 s1, s0, 31
	s_lshl_b64 s[0:1], s[0:1], 1
	s_add_u32 s0, s10, s0
	s_addc_u32 s1, s9, s1
	v_lshl_add_u64 v[6:7], s[0:1], 0, v[2:3]
	global_load_dword v12, v2, s[0:1] offset:3072
	v_add_co_u32_e64 v10, s[0:1], s20, v6
	s_nop 1
	v_addc_co_u32_e64 v11, s[0:1], 0, v7, s[0:1]
	s_movk_i32 s0, 0x6000
	global_load_dword v13, v[10:11], off offset:3072
	v_add_co_u32_e64 v10, s[0:1], s0, v6
	s_nop 1
	v_addc_co_u32_e64 v11, s[0:1], 0, v7, s[0:1]
	s_mov_b32 s0, 0x9000
	global_load_dword v14, v[10:11], off offset:3072
	v_add_co_u32_e64 v10, s[0:1], s0, v6
	s_nop 1
	v_addc_co_u32_e64 v11, s[0:1], 0, v7, s[0:1]
	s_mov_b32 s0, 0xc000
	global_load_dword v15, v[10:11], off offset:3072
	v_add_co_u32_e64 v10, s[0:1], s0, v6
	s_nop 1
	v_addc_co_u32_e64 v11, s[0:1], 0, v7, s[0:1]
	s_mov_b32 s0, 0xf000
	global_load_dword v17, v[10:11], off offset:3072
	v_add_co_u32_e64 v10, s[0:1], s0, v6
	s_nop 1
	v_addc_co_u32_e64 v11, s[0:1], 0, v7, s[0:1]
	s_mov_b32 s0, 0x12000
	global_load_dword v19, v[10:11], off offset:3072
	v_add_co_u32_e64 v10, s[0:1], s0, v6
	s_nop 1
	v_addc_co_u32_e64 v11, s[0:1], 0, v7, s[0:1]
	s_mov_b32 s0, 0x15000
	global_load_dword v21, v[10:11], off offset:3072
	v_add_co_u32_e64 v10, s[0:1], s0, v6
	s_nop 1
	v_addc_co_u32_e64 v11, s[0:1], 0, v7, s[0:1]
	s_mov_b32 s0, 0x18000
	global_load_dword v23, v[10:11], off offset:3072
	v_add_co_u32_e64 v10, s[0:1], s0, v6
	s_nop 1
	v_addc_co_u32_e64 v11, s[0:1], 0, v7, s[0:1]
	s_mov_b32 s0, 0x1b000
	global_load_dword v25, v[10:11], off offset:3072
	v_add_co_u32_e64 v10, s[0:1], s0, v6
	s_nop 1
	v_addc_co_u32_e64 v11, s[0:1], 0, v7, s[0:1]
	s_mov_b32 s0, 0x1e000
	global_load_dword v27, v[10:11], off offset:3072
	v_add_co_u32_e64 v10, s[0:1], s0, v6
	s_nop 1
	v_addc_co_u32_e64 v11, s[0:1], 0, v7, s[0:1]
	s_mov_b32 s0, 0x21000
	global_load_dword v28, v[10:11], off offset:3072
	v_add_co_u32_e64 v10, s[0:1], s0, v6
	s_nop 1
	v_addc_co_u32_e64 v11, s[0:1], 0, v7, s[0:1]
	s_mov_b32 s0, 0x24000
	global_load_dword v29, v[10:11], off offset:3072
	v_add_co_u32_e64 v10, s[0:1], s0, v6
	s_nop 1
	v_addc_co_u32_e64 v11, s[0:1], 0, v7, s[0:1]
	s_mov_b32 s0, 0x27000
	global_load_dword v30, v[10:11], off offset:3072
	v_add_co_u32_e64 v10, s[0:1], s0, v6
	s_nop 1
	v_addc_co_u32_e64 v11, s[0:1], 0, v7, s[0:1]
	s_mov_b32 s0, 0x2a000
	global_load_dword v31, v[10:11], off offset:3072
	v_add_co_u32_e64 v10, s[0:1], s0, v6
	s_nop 1
	v_addc_co_u32_e64 v11, s[0:1], 0, v7, s[0:1]
	s_mov_b32 s0, 0x2d000
	global_load_dword v32, v[10:11], off offset:3072
	v_add_co_u32_e64 v10, s[0:1], s0, v6
	s_nop 1
	v_addc_co_u32_e64 v11, s[0:1], 0, v7, s[0:1]
	s_mov_b32 s0, 0x30000
	global_load_dword v33, v[10:11], off offset:3072
	v_add_co_u32_e64 v10, s[0:1], s0, v6
	s_nop 1
	v_addc_co_u32_e64 v11, s[0:1], 0, v7, s[0:1]
	s_mov_b32 s0, 0x33000
	global_load_dword v34, v[10:11], off offset:3072
	v_add_co_u32_e64 v10, s[0:1], s0, v6
	s_nop 1
	v_addc_co_u32_e64 v11, s[0:1], 0, v7, s[0:1]
	s_mov_b32 s0, 0x36000
	global_load_dword v35, v[10:11], off offset:3072
	v_add_co_u32_e64 v10, s[0:1], s0, v6
	s_nop 1
	v_addc_co_u32_e64 v11, s[0:1], 0, v7, s[0:1]
	s_mov_b32 s0, 0x39000
	global_load_dword v36, v[10:11], off offset:3072
	v_add_co_u32_e64 v10, s[0:1], s0, v6
	s_nop 1
	v_addc_co_u32_e64 v11, s[0:1], 0, v7, s[0:1]
	s_mov_b32 s0, 0x3c000
	global_load_dword v37, v[10:11], off offset:3072
	v_add_co_u32_e64 v10, s[0:1], s0, v6
	s_nop 1
	v_addc_co_u32_e64 v11, s[0:1], 0, v7, s[0:1]
	s_mov_b32 s0, 0x3f000
	global_load_dword v38, v[10:11], off offset:3072
	v_add_co_u32_e64 v10, s[0:1], s0, v6
	s_nop 1
	v_addc_co_u32_e64 v11, s[0:1], 0, v7, s[0:1]
	s_mov_b32 s0, 0x42000
	global_load_dword v39, v[10:11], off offset:3072
	v_add_co_u32_e64 v10, s[0:1], s0, v6
	s_nop 1
	v_addc_co_u32_e64 v11, s[0:1], 0, v7, s[0:1]
	s_mov_b32 s0, 0x45000
	global_load_dword v40, v[10:11], off offset:3072
	v_add_co_u32_e64 v10, s[0:1], s0, v6
	s_nop 1
	v_addc_co_u32_e64 v11, s[0:1], 0, v7, s[0:1]
	s_mov_b32 s0, 0x48000
	global_load_dword v41, v[10:11], off offset:3072
	v_add_co_u32_e64 v10, s[0:1], s0, v6
	s_nop 1
	v_addc_co_u32_e64 v11, s[0:1], 0, v7, s[0:1]
	s_mov_b32 s0, 0x4b000
	global_load_dword v42, v[10:11], off offset:3072
	v_add_co_u32_e64 v10, s[0:1], s0, v6
	s_nop 1
	v_addc_co_u32_e64 v11, s[0:1], 0, v7, s[0:1]
	s_mov_b32 s0, 0x4e000
	global_load_dword v43, v[10:11], off offset:3072
	v_add_co_u32_e64 v10, s[0:1], s0, v6
	s_nop 1
	v_addc_co_u32_e64 v11, s[0:1], 0, v7, s[0:1]
	s_mov_b32 s0, 0x51000
	global_load_dword v44, v[10:11], off offset:3072
	v_add_co_u32_e64 v10, s[0:1], s0, v6
	s_nop 1
	v_addc_co_u32_e64 v11, s[0:1], 0, v7, s[0:1]
	s_mov_b32 s0, 0x54000
	global_load_dword v45, v[10:11], off offset:3072
	v_add_co_u32_e64 v10, s[0:1], s0, v6
	s_nop 1
	v_addc_co_u32_e64 v11, s[0:1], 0, v7, s[0:1]
	s_mov_b32 s0, 0x57000
	global_load_dword v46, v[10:11], off offset:3072
	v_add_co_u32_e64 v10, s[0:1], s0, v6
	s_nop 1
	v_addc_co_u32_e64 v11, s[0:1], 0, v7, s[0:1]
	s_mov_b32 s0, 0x5a000
	global_load_dword v47, v[10:11], off offset:3072
	v_add_co_u32_e64 v10, s[0:1], s0, v6
	s_nop 1
	v_addc_co_u32_e64 v11, s[0:1], 0, v7, s[0:1]
	s_mov_b32 s0, 0x5d000
	s_nop 0
	v_add_co_u32_e64 v6, s[0:1], s0, v6
	global_load_dword v48, v[10:11], off offset:3072
	s_nop 0
	v_addc_co_u32_e64 v7, s[0:1], 0, v7, s[0:1]
	global_load_dword v49, v[6:7], off offset:3072
	s_waitcnt vmcnt(22)
	v_lshlrev_b32_e32 v16, 16, v17
	v_and_b32_e32 v17, 0xffff0000, v17
	v_lshlrev_b32_e32 v18, 16, v19
	v_and_b32_e32 v19, 0xffff0000, v19
	v_lshlrev_b32_e32 v20, 16, v21
	v_and_b32_e32 v21, 0xffff0000, v21
	v_lshlrev_b32_e32 v22, 16, v23
	v_and_b32_e32 v23, 0xffff0000, v23
	v_lshlrev_b32_e32 v24, 16, v25
	v_and_b32_e32 v25, 0xffff0000, v25
	v_lshlrev_b32_e32 v26, 16, v27
	v_and_b32_e32 v27, 0xffff0000, v27
	v_lshlrev_b32_e32 v6, 16, v12
	v_and_b32_e32 v7, 0xffff0000, v12
	v_lshlrev_b32_e32 v10, 16, v13
	v_and_b32_e32 v11, 0xffff0000, v13
	v_pk_add_f32 v[6:7], v[6:7], 0 op_sel_hi:[1,0]
	v_lshlrev_b32_e32 v12, 16, v14
	v_and_b32_e32 v13, 0xffff0000, v14
	v_pk_add_f32 v[6:7], v[6:7], v[10:11]
	v_lshlrev_b32_e32 v14, 16, v15
	v_and_b32_e32 v15, 0xffff0000, v15
	v_pk_add_f32 v[6:7], v[6:7], v[12:13]
	s_waitcnt vmcnt(21)
	v_lshlrev_b32_e32 v10, 16, v28
	v_pk_add_f32 v[6:7], v[6:7], v[14:15]
	v_and_b32_e32 v11, 0xffff0000, v28
	v_pk_add_f32 v[6:7], v[6:7], v[16:17]
	s_waitcnt vmcnt(20)
	v_lshlrev_b32_e32 v12, 16, v29
	v_pk_add_f32 v[6:7], v[6:7], v[18:19]
	v_and_b32_e32 v13, 0xffff0000, v29
	v_pk_add_f32 v[6:7], v[6:7], v[20:21]
	s_waitcnt vmcnt(19)
	v_lshlrev_b32_e32 v14, 16, v30
	v_pk_add_f32 v[6:7], v[6:7], v[22:23]
	v_and_b32_e32 v15, 0xffff0000, v30
	v_pk_add_f32 v[6:7], v[6:7], v[24:25]
	s_waitcnt vmcnt(18)
	v_lshlrev_b32_e32 v16, 16, v31
	v_pk_add_f32 v[6:7], v[6:7], v[26:27]
	v_and_b32_e32 v17, 0xffff0000, v31
	v_pk_add_f32 v[6:7], v[6:7], v[10:11]
	s_waitcnt vmcnt(17)
	v_lshlrev_b32_e32 v18, 16, v32
	v_pk_add_f32 v[6:7], v[6:7], v[12:13]
	v_and_b32_e32 v19, 0xffff0000, v32
	v_pk_add_f32 v[6:7], v[6:7], v[14:15]
	s_waitcnt vmcnt(16)
	v_lshlrev_b32_e32 v20, 16, v33
	v_pk_add_f32 v[6:7], v[6:7], v[16:17]
	v_and_b32_e32 v21, 0xffff0000, v33
	v_pk_add_f32 v[6:7], v[6:7], v[18:19]
	s_waitcnt vmcnt(15)
	v_lshlrev_b32_e32 v22, 16, v34
	v_and_b32_e32 v23, 0xffff0000, v34
	v_pk_add_f32 v[6:7], v[6:7], v[20:21]
	s_waitcnt vmcnt(14)
	v_lshlrev_b32_e32 v24, 16, v35
	v_and_b32_e32 v25, 0xffff0000, v35
	v_pk_add_f32 v[6:7], v[6:7], v[22:23]
	s_waitcnt vmcnt(13)
	v_lshlrev_b32_e32 v26, 16, v36
	v_and_b32_e32 v27, 0xffff0000, v36
	v_pk_add_f32 v[6:7], v[6:7], v[24:25]
	s_waitcnt vmcnt(12)
	v_lshlrev_b32_e32 v28, 16, v37
	v_and_b32_e32 v29, 0xffff0000, v37
	v_pk_add_f32 v[6:7], v[6:7], v[26:27]
	s_waitcnt vmcnt(11)
	v_lshlrev_b32_e32 v30, 16, v38
	v_and_b32_e32 v31, 0xffff0000, v38
	v_pk_add_f32 v[6:7], v[6:7], v[28:29]
	s_waitcnt vmcnt(10)
	v_lshlrev_b32_e32 v10, 16, v39
	v_pk_add_f32 v[6:7], v[6:7], v[30:31]
	v_and_b32_e32 v11, 0xffff0000, v39
	s_waitcnt vmcnt(9)
	v_lshlrev_b32_e32 v12, 16, v40
	v_and_b32_e32 v13, 0xffff0000, v40
	v_pk_add_f32 v[6:7], v[6:7], v[10:11]
	s_waitcnt vmcnt(8)
	v_lshlrev_b32_e32 v14, 16, v41
	v_and_b32_e32 v15, 0xffff0000, v41
	v_pk_add_f32 v[6:7], v[6:7], v[12:13]
	s_waitcnt vmcnt(7)
	v_lshlrev_b32_e32 v16, 16, v42
	v_and_b32_e32 v17, 0xffff0000, v42
	v_pk_add_f32 v[6:7], v[6:7], v[14:15]
	s_waitcnt vmcnt(6)
	v_lshlrev_b32_e32 v18, 16, v43
	v_and_b32_e32 v19, 0xffff0000, v43
	v_pk_add_f32 v[6:7], v[6:7], v[16:17]
	s_waitcnt vmcnt(5)
	v_lshlrev_b32_e32 v20, 16, v44
	v_and_b32_e32 v21, 0xffff0000, v44
	v_pk_add_f32 v[6:7], v[6:7], v[18:19]
	s_waitcnt vmcnt(4)
	v_lshlrev_b32_e32 v22, 16, v45
	v_and_b32_e32 v23, 0xffff0000, v45
	v_pk_add_f32 v[6:7], v[6:7], v[20:21]
	s_waitcnt vmcnt(3)
	v_lshlrev_b32_e32 v24, 16, v46
	v_and_b32_e32 v25, 0xffff0000, v46
	v_pk_add_f32 v[6:7], v[6:7], v[22:23]
	s_waitcnt vmcnt(2)
	v_lshlrev_b32_e32 v26, 16, v47
	v_and_b32_e32 v27, 0xffff0000, v47
	v_pk_add_f32 v[6:7], v[6:7], v[24:25]
	s_waitcnt vmcnt(1)
	v_lshlrev_b32_e32 v28, 16, v48
	v_and_b32_e32 v29, 0xffff0000, v48
	v_pk_add_f32 v[6:7], v[6:7], v[26:27]
	s_waitcnt vmcnt(0)
	v_lshlrev_b32_e32 v30, 16, v49
	v_and_b32_e32 v31, 0xffff0000, v49
	v_pk_add_f32 v[6:7], v[6:7], v[28:29]
	s_nop 0
	v_pk_add_f32 v[6:7], v[6:7], v[30:31]
	ds_write_b64 v9, v[6:7]
	s_waitcnt lgkmcnt(0)
	s_barrier
	s_and_saveexec_b64 s[0:1], vcc
	s_cbranch_execz .LBB0_416
	ds_read2st64_b32 v[6:7], v8 offset1:2
	s_lshl_b64 s[10:11], s[4:5], 9
	s_waitcnt lgkmcnt(0)
	v_add_f32_e32 v6, 0, v6
	v_add_f32_e32 v10, v6, v7
	ds_read2st64_b32 v[6:7], v8 offset0:4 offset1:6
	s_waitcnt lgkmcnt(0)
	v_add_f32_e32 v6, v10, v6
	v_add_f32_e32 v10, v6, v7
	ds_read2st64_b32 v[6:7], v8 offset0:8 offset1:10
	s_waitcnt lgkmcnt(0)
	v_add_f32_e32 v6, v10, v6
	v_add_f32_e32 v10, v6, v7
	ds_read2st64_b32 v[6:7], v8 offset0:12 offset1:14
	s_waitcnt lgkmcnt(0)
	v_add_f32_e32 v6, v10, v6
	v_add_f32_e32 v6, v6, v7
	v_mul_f32_e32 v10, 0x3b800000, v6
	v_lshl_add_u64 v[6:7], v[4:5], 0, s[10:11]
	global_store_dword v[6:7], v10, off
	s_branch .LBB0_416
